# baseline (speedup 1.0000x reference)
.LBB2_169:
	ds_read_u16 v0, v102
	s_waitcnt lgkmcnt(0)
	v_and_b32_e32 v105, 0xffff, v0
	v_lshrrev_b32_e32 v250, 11, v105
	v_bfe_u32 v251, v105, 8, 3
	v_mad_u32_u24 v250, v250, 10, v251
	v_lshlrev_b32_e32 v250, 9, v250
	v_lshl_add_u32 v250, v97, 4, v250
	v_add_u32_e32 v250, 0x13e00, v250
	v_mul_lo_u16_sdwa v0, v0, s6 dst_sel:DWORD dst_unused:UNUSED_PAD src0_sel:BYTE_0 src1_sel:DWORD
	v_lshrrev_b32_e32 v50, 11, v105
	v_bfe_u32 v54, v105, 8, 3
	v_lshrrev_b16_e32 v52, 10, v0
	v_and_b32_e32 v104, 0xff, v105
	v_add_u32_e32 v55, s12, v54
	v_mul_i32_i24_e32 v0, -13, v52
	v_add_u32_e32 v56, s11, v50
	v_add3_u32 v57, v104, v96, v0
	v_add_lshl_u32 v60, s10, v52, 6
	v_add_u32_e32 v52, v57, v60
	v_ashrrev_i32_e32 v53, 31, v52
	v_lshlrev_b64 v[52:53], 9, v[52:53]
	v_lshl_add_u64 v[52:53], v[90:91], 0, v[52:53]
	ds_read_b128 v[106:109], v250 offset:256
	ds_read_b128 v[70:73], v250
	global_load_dwordx4 v[116:119], v[52:53], off offset:16
	global_load_dwordx4 v[120:123], v[52:53], off
	v_add_u32_e32 v61, 1, v57
	v_add_u32_e32 v52, v61, v60
	v_ashrrev_i32_e32 v53, 31, v52
	v_lshlrev_b64 v[52:53], 9, v[52:53]
	v_lshl_add_u64 v[52:53], v[90:91], 0, v[52:53]
	ds_read_b128 v[124:127], v250 offset:768
	ds_read_b128 v[128:131], v250 offset:512
	global_load_dwordx4 v[132:135], v[52:53], off offset:16
	global_load_dwordx4 v[136:139], v[52:53], off
	v_max_i32_e32 v0, -2, v55
	v_add_u32_e32 v0, 2, v0
	v_min_u32_e32 v0, 63, v0
	v_add_u32_e32 v64, 2, v57
	v_lshlrev_b32_e32 v62, 9, v0
	v_add_u32_e32 v52, v64, v60
	v_ashrrev_i32_e32 v53, 31, v52
	v_lshlrev_b64 v[52:53], 9, v[52:53]
	v_lshl_add_u64 v[52:53], v[90:91], 0, v[52:53]
	ds_read_b128 v[140:143], v250 offset:1280
	ds_read_b128 v[144:147], v250 offset:1024
	global_load_dwordx4 v[148:151], v[52:53], off offset:16
	global_load_dwordx4 v[152:155], v[52:53], off
	v_add_u32_e32 v58, 64, v60
	v_add_u32_e32 v52, v57, v58
	v_ashrrev_i32_e32 v53, 31, v52
	v_lshlrev_b64 v[52:53], 9, v[52:53]
	v_lshl_add_u64 v[52:53], v[90:91], 0, v[52:53]
	ds_read_b128 v[156:159], v250 offset:5376
	ds_read_b128 v[160:163], v250 offset:5120
	global_load_dwordx4 v[164:167], v[52:53], off offset:16
	global_load_dwordx4 v[168:171], v[52:53], off
	v_add_u32_e32 v52, v61, v58
	v_ashrrev_i32_e32 v53, 31, v52
	v_lshlrev_b64 v[52:53], 9, v[52:53]
	v_lshl_add_u64 v[52:53], v[90:91], 0, v[52:53]
	ds_read_b128 v[172:175], v250 offset:5888
	ds_read_b128 v[176:179], v250 offset:5632
	global_load_dwordx4 v[180:183], v[52:53], off offset:16
	global_load_dwordx4 v[184:187], v[52:53], off
	v_add_u32_e32 v52, v64, v58
	v_ashrrev_i32_e32 v53, 31, v52
	v_lshlrev_b64 v[52:53], 9, v[52:53]
	v_lshl_add_u64 v[52:53], v[90:91], 0, v[52:53]
	ds_read_b128 v[188:191], v250 offset:6400
	ds_read_b128 v[192:195], v250 offset:6144
	global_load_dwordx4 v[196:199], v[52:53], off offset:16
	global_load_dwordx4 v[200:203], v[52:53], off
	v_max_i32_e32 v0, -2, v56
	v_add_u32_e32 v0, 2, v0
	v_min_u32_e32 v0, 63, v0
	v_add_u32_e32 v65, 0x80, v60
	v_lshlrev_b32_e32 v63, 15, v0
	v_add_u32_e32 v52, v57, v65
	v_ashrrev_i32_e32 v53, 31, v52
	v_lshlrev_b64 v[52:53], 9, v[52:53]
	v_lshl_add_u64 v[52:53], v[90:91], 0, v[52:53]
	ds_read_b128 v[74:77], v250 offset:10496
	ds_read_b128 v[204:207], v250 offset:10240
	global_load_dwordx4 v[82:85], v[52:53], off offset:16
	global_load_dwordx4 v[208:211], v[52:53], off
	v_add_u32_e32 v52, v61, v65
	v_ashrrev_i32_e32 v53, 31, v52
	v_lshlrev_b64 v[52:53], 9, v[52:53]
	v_lshl_add_u64 v[52:53], v[90:91], 0, v[52:53]
	s_waitcnt lgkmcnt(13)
	ds_read_b128 v[54:57], v250 offset:11008
	ds_read_b128 v[66:69], v250 offset:10752
	global_load_dwordx4 v[58:61], v[52:53], off offset:16
	global_load_dwordx4 v[78:81], v[52:53], off
	v_add_u32_e32 v50, v64, v65
	v_ashrrev_i32_e32 v51, 31, v50
	v_lshlrev_b64 v[50:51], 9, v[50:51]
	v_lshl_add_u64 v[110:111], v[90:91], 0, v[50:51]
	v_or_b32_e32 v0, v63, v62
	s_waitcnt lgkmcnt(13)
	v_cvt_f64_f32_e32 v[50:51], v70
	s_waitcnt vmcnt(14)
	v_cvt_f64_f32_e32 v[52:53], v120
	v_fma_f64 v[92:93], v[50:51], v[52:53], 0
	v_cvt_f64_f32_e32 v[50:51], v72
	v_cvt_f64_f32_e32 v[52:53], v122
	v_fmac_f64_e32 v[92:93], v[50:51], v[52:53]
	v_cvt_f64_f32_e32 v[50:51], v71
	v_cvt_f64_f32_e32 v[52:53], v121
	v_fma_f64 v[94:95], v[50:51], v[52:53], 0
	v_cvt_f64_f32_e32 v[70:71], v73
	v_cvt_f64_f32_e32 v[72:73], v123
	v_fmac_f64_e32 v[94:95], v[70:71], v[72:73]
	v_cvt_f64_f32_e32 v[70:71], v106
	v_cvt_f64_f32_e32 v[72:73], v116
	v_fmac_f64_e32 v[92:93], v[70:71], v[72:73]
	v_cvt_f64_f32_e32 v[70:71], v107
	v_cvt_f64_f32_e32 v[72:73], v117
	v_fmac_f64_e32 v[94:95], v[70:71], v[72:73]
	v_cvt_f64_f32_e32 v[70:71], v108
	v_cvt_f64_f32_e32 v[72:73], v118
	s_waitcnt lgkmcnt(13)
	ds_read_b128 v[50:53], v250 offset:11520
	s_nop 0
	ds_read_b128 v[62:65], v250 offset:11264
	v_fmac_f64_e32 v[92:93], v[70:71], v[72:73]
	global_load_dwordx4 v[70:73], v[110:111], off offset:16
	global_load_dwordx4 v[120:123], v[110:111], off
	v_cvt_f64_f32_e32 v[106:107], v109
	v_cvt_f64_f32_e32 v[108:109], v119
	v_fmac_f64_e32 v[94:95], v[106:107], v[108:109]
	s_waitcnt lgkmcnt(13)
	v_cvt_f64_f32_e32 v[106:107], v128
	s_waitcnt vmcnt(14)
	v_cvt_f64_f32_e32 v[108:109], v136
	v_fmac_f64_e32 v[92:93], v[106:107], v[108:109]
	v_cvt_f64_f32_e32 v[106:107], v129
	v_cvt_f64_f32_e32 v[108:109], v137
	v_fmac_f64_e32 v[94:95], v[106:107], v[108:109]
	v_cvt_f64_f32_e32 v[106:107], v130
	v_cvt_f64_f32_e32 v[108:109], v138
	v_fmac_f64_e32 v[92:93], v[106:107], v[108:109]
	v_cvt_f64_f32_e32 v[106:107], v131
	v_cvt_f64_f32_e32 v[108:109], v139
	v_fmac_f64_e32 v[94:95], v[106:107], v[108:109]
	v_cvt_f64_f32_e32 v[106:107], v124
	v_cvt_f64_f32_e32 v[108:109], v132
	v_fmac_f64_e32 v[92:93], v[106:107], v[108:109]
	v_cvt_f64_f32_e32 v[106:107], v125
	v_cvt_f64_f32_e32 v[108:109], v133
	v_fmac_f64_e32 v[94:95], v[106:107], v[108:109]
	v_cvt_f64_f32_e32 v[106:107], v126
	v_cvt_f64_f32_e32 v[108:109], v134
	v_fmac_f64_e32 v[92:93], v[106:107], v[108:109]
	v_cvt_f64_f32_e32 v[106:107], v127
	v_cvt_f64_f32_e32 v[108:109], v135
	v_fmac_f64_e32 v[94:95], v[106:107], v[108:109]
	s_waitcnt lgkmcnt(12)
	v_cvt_f64_f32_e32 v[106:107], v144
	s_waitcnt vmcnt(12)
	v_cvt_f64_f32_e32 v[108:109], v152
	v_fmac_f64_e32 v[92:93], v[106:107], v[108:109]
	v_cvt_f64_f32_e32 v[106:107], v145
	v_cvt_f64_f32_e32 v[108:109], v153
	v_fmac_f64_e32 v[94:95], v[106:107], v[108:109]
	v_cvt_f64_f32_e32 v[106:107], v146
	v_cvt_f64_f32_e32 v[108:109], v154
	v_fmac_f64_e32 v[92:93], v[106:107], v[108:109]
	v_cvt_f64_f32_e32 v[106:107], v147
	v_cvt_f64_f32_e32 v[108:109], v155
	v_fmac_f64_e32 v[94:95], v[106:107], v[108:109]
	v_cvt_f64_f32_e32 v[106:107], v140
	v_cvt_f64_f32_e32 v[108:109], v148
	v_fmac_f64_e32 v[92:93], v[106:107], v[108:109]
	v_cvt_f64_f32_e32 v[106:107], v141
	v_cvt_f64_f32_e32 v[108:109], v149
	v_fmac_f64_e32 v[94:95], v[106:107], v[108:109]
	v_cvt_f64_f32_e32 v[106:107], v142
	v_cvt_f64_f32_e32 v[108:109], v150
	v_fmac_f64_e32 v[92:93], v[106:107], v[108:109]
	v_cvt_f64_f32_e32 v[106:107], v143
	v_cvt_f64_f32_e32 v[108:109], v151
	v_fmac_f64_e32 v[94:95], v[106:107], v[108:109]
	s_waitcnt lgkmcnt(10)
	v_cvt_f64_f32_e32 v[106:107], v160
	s_waitcnt vmcnt(10)
	v_cvt_f64_f32_e32 v[108:109], v168
	v_fmac_f64_e32 v[92:93], v[106:107], v[108:109]
	v_cvt_f64_f32_e32 v[106:107], v161
	v_cvt_f64_f32_e32 v[108:109], v169
	v_fmac_f64_e32 v[94:95], v[106:107], v[108:109]
	v_cvt_f64_f32_e32 v[106:107], v162
	v_cvt_f64_f32_e32 v[108:109], v170
	v_fmac_f64_e32 v[92:93], v[106:107], v[108:109]
	v_cvt_f64_f32_e32 v[106:107], v163
	v_cvt_f64_f32_e32 v[108:109], v171
	v_fmac_f64_e32 v[94:95], v[106:107], v[108:109]
	v_cvt_f64_f32_e32 v[106:107], v156
	v_cvt_f64_f32_e32 v[108:109], v164
	v_fmac_f64_e32 v[92:93], v[106:107], v[108:109]
	v_cvt_f64_f32_e32 v[106:107], v157
	v_cvt_f64_f32_e32 v[108:109], v165
	v_fmac_f64_e32 v[94:95], v[106:107], v[108:109]
	v_cvt_f64_f32_e32 v[106:107], v158
	v_cvt_f64_f32_e32 v[108:109], v166
	v_fmac_f64_e32 v[92:93], v[106:107], v[108:109]
	v_cvt_f64_f32_e32 v[106:107], v159
	v_cvt_f64_f32_e32 v[108:109], v167
	v_fmac_f64_e32 v[94:95], v[106:107], v[108:109]
	s_waitcnt lgkmcnt(8)
	v_cvt_f64_f32_e32 v[106:107], v176
	s_waitcnt vmcnt(8)
	v_cvt_f64_f32_e32 v[108:109], v184
	v_fmac_f64_e32 v[92:93], v[106:107], v[108:109]
	v_cvt_f64_f32_e32 v[106:107], v177
	v_cvt_f64_f32_e32 v[108:109], v185
	v_fmac_f64_e32 v[94:95], v[106:107], v[108:109]
	v_cvt_f64_f32_e32 v[106:107], v178
	v_cvt_f64_f32_e32 v[108:109], v186
	v_fmac_f64_e32 v[92:93], v[106:107], v[108:109]
	v_cvt_f64_f32_e32 v[106:107], v179
	v_cvt_f64_f32_e32 v[108:109], v187
	v_fmac_f64_e32 v[94:95], v[106:107], v[108:109]
	v_cvt_f64_f32_e32 v[106:107], v172
	v_cvt_f64_f32_e32 v[108:109], v180
	v_fmac_f64_e32 v[92:93], v[106:107], v[108:109]
	v_cvt_f64_f32_e32 v[106:107], v173
	v_cvt_f64_f32_e32 v[108:109], v181
	v_fmac_f64_e32 v[94:95], v[106:107], v[108:109]
	v_cvt_f64_f32_e32 v[106:107], v174
	v_cvt_f64_f32_e32 v[108:109], v182
	v_fmac_f64_e32 v[92:93], v[106:107], v[108:109]
	v_cvt_f64_f32_e32 v[106:107], v175
	v_cvt_f64_f32_e32 v[108:109], v183
	v_fmac_f64_e32 v[94:95], v[106:107], v[108:109]
	s_waitcnt lgkmcnt(6)
	v_cvt_f64_f32_e32 v[106:107], v192
	s_waitcnt vmcnt(6)
	v_cvt_f64_f32_e32 v[108:109], v200
	v_fmac_f64_e32 v[92:93], v[106:107], v[108:109]
	v_cvt_f64_f32_e32 v[106:107], v193
	v_cvt_f64_f32_e32 v[108:109], v201
	v_fmac_f64_e32 v[94:95], v[106:107], v[108:109]
	v_cvt_f64_f32_e32 v[106:107], v194
	v_cvt_f64_f32_e32 v[108:109], v202
	v_fmac_f64_e32 v[92:93], v[106:107], v[108:109]
	v_cvt_f64_f32_e32 v[106:107], v195
	v_cvt_f64_f32_e32 v[108:109], v203
	v_fmac_f64_e32 v[94:95], v[106:107], v[108:109]
	v_cvt_f64_f32_e32 v[106:107], v188
	v_cvt_f64_f32_e32 v[108:109], v196
	v_fmac_f64_e32 v[92:93], v[106:107], v[108:109]
	v_cvt_f64_f32_e32 v[106:107], v189
	v_cvt_f64_f32_e32 v[108:109], v197
	v_fmac_f64_e32 v[94:95], v[106:107], v[108:109]
	v_cvt_f64_f32_e32 v[106:107], v190
	v_cvt_f64_f32_e32 v[108:109], v198
	v_fmac_f64_e32 v[92:93], v[106:107], v[108:109]
	v_cvt_f64_f32_e32 v[106:107], v191
	v_cvt_f64_f32_e32 v[108:109], v199
	v_fmac_f64_e32 v[94:95], v[106:107], v[108:109]
	s_waitcnt lgkmcnt(4)
	v_cvt_f64_f32_e32 v[106:107], v204
	s_waitcnt vmcnt(4)
	v_cvt_f64_f32_e32 v[108:109], v208
	v_fmac_f64_e32 v[92:93], v[106:107], v[108:109]
	v_cvt_f64_f32_e32 v[106:107], v205
	v_cvt_f64_f32_e32 v[108:109], v209
	v_fmac_f64_e32 v[94:95], v[106:107], v[108:109]
	v_cvt_f64_f32_e32 v[106:107], v206
	v_cvt_f64_f32_e32 v[108:109], v210
	v_fmac_f64_e32 v[92:93], v[106:107], v[108:109]
	v_cvt_f64_f32_e32 v[106:107], v207
	v_cvt_f64_f32_e32 v[108:109], v211
	v_fmac_f64_e32 v[94:95], v[106:107], v[108:109]
	v_cvt_f64_f32_e32 v[106:107], v74
	v_cvt_f64_f32_e32 v[108:109], v82
	v_cvt_f64_f32_e32 v[74:75], v75
	v_cvt_f64_f32_e32 v[82:83], v83
	v_fmac_f64_e32 v[92:93], v[106:107], v[108:109]
	v_fmac_f64_e32 v[94:95], v[74:75], v[82:83]
	v_cvt_f64_f32_e32 v[74:75], v76
	v_cvt_f64_f32_e32 v[82:83], v84
	v_fmac_f64_e32 v[92:93], v[74:75], v[82:83]
	v_cvt_f64_f32_e32 v[74:75], v77
	v_cvt_f64_f32_e32 v[76:77], v85
	v_fmac_f64_e32 v[94:95], v[74:75], v[76:77]
	s_waitcnt lgkmcnt(2)
	v_cvt_f64_f32_e32 v[74:75], v66
	s_waitcnt vmcnt(2)
	v_cvt_f64_f32_e32 v[76:77], v78
	v_fmac_f64_e32 v[92:93], v[74:75], v[76:77]
	v_cvt_f64_f32_e32 v[66:67], v67
	v_cvt_f64_f32_e32 v[74:75], v79
	v_fmac_f64_e32 v[94:95], v[66:67], v[74:75]
	v_cvt_f64_f32_e32 v[66:67], v68
	v_cvt_f64_f32_e32 v[74:75], v80
	v_fmac_f64_e32 v[92:93], v[66:67], v[74:75]
	v_cvt_f64_f32_e32 v[66:67], v69
	v_cvt_f64_f32_e32 v[68:69], v81
	v_fmac_f64_e32 v[94:95], v[66:67], v[68:69]
	v_cvt_f64_f32_e32 v[66:67], v54
	v_cvt_f64_f32_e32 v[68:69], v58
	v_cvt_f64_f32_e32 v[54:55], v55
	v_cvt_f64_f32_e32 v[58:59], v59
	v_fmac_f64_e32 v[92:93], v[66:67], v[68:69]
	v_fmac_f64_e32 v[94:95], v[54:55], v[58:59]
	v_cvt_f64_f32_e32 v[54:55], v56
	v_cvt_f64_f32_e32 v[58:59], v60
	v_fmac_f64_e32 v[92:93], v[54:55], v[58:59]
	v_cvt_f64_f32_e32 v[54:55], v57
	v_cvt_f64_f32_e32 v[56:57], v61
	v_fmac_f64_e32 v[94:95], v[54:55], v[56:57]
	s_waitcnt lgkmcnt(0)
	v_cvt_f64_f32_e32 v[54:55], v62
	s_waitcnt vmcnt(0)
	v_cvt_f64_f32_e32 v[56:57], v120
	v_fmac_f64_e32 v[92:93], v[54:55], v[56:57]
	v_cvt_f64_f32_e32 v[54:55], v63
	v_cvt_f64_f32_e32 v[56:57], v121
	v_fmac_f64_e32 v[94:95], v[54:55], v[56:57]
	v_cvt_f64_f32_e32 v[54:55], v64
	v_cvt_f64_f32_e32 v[56:57], v122
	v_fmac_f64_e32 v[92:93], v[54:55], v[56:57]
	v_cvt_f64_f32_e32 v[54:55], v65
	v_cvt_f64_f32_e32 v[56:57], v123
	v_fmac_f64_e32 v[94:95], v[54:55], v[56:57]
	v_cvt_f64_f32_e32 v[54:55], v50
	v_cvt_f64_f32_e32 v[56:57], v70
	v_fmac_f64_e32 v[92:93], v[54:55], v[56:57]
	v_cvt_f64_f32_e32 v[50:51], v51
	v_cvt_f64_f32_e32 v[54:55], v71
	v_fmac_f64_e32 v[94:95], v[50:51], v[54:55]
	v_cvt_f64_f32_e32 v[50:51], v52
	v_cvt_f64_f32_e32 v[54:55], v72
	v_fmac_f64_e32 v[92:93], v[50:51], v[54:55]
	v_cvt_f64_f32_e32 v[50:51], v53
	v_cvt_f64_f32_e32 v[52:53], v73
	v_fmac_f64_e32 v[94:95], v[50:51], v[52:53]
	v_add_f64 v[50:51], v[92:93], v[94:95]
	s_nop 1
	v_mov_b32_dpp v52, v50 quad_perm:[1,0,3,2] row_mask:0xf bank_mask:0xf
	v_mov_b32_dpp v53, v51 quad_perm:[1,0,3,2] row_mask:0xf bank_mask:0xf
	s_waitcnt lgkmcnt(0)
	v_add_f64 v[50:51], v[50:51], v[52:53]
	s_nop 1
	v_mov_b32_dpp v52, v50 quad_perm:[2,3,0,1] row_mask:0xf bank_mask:0xf
	v_mov_b32_dpp v53, v51 quad_perm:[2,3,0,1] row_mask:0xf bank_mask:0xf
	s_waitcnt lgkmcnt(0)
	v_add_f64 v[50:51], v[50:51], v[52:53]
	s_nop 1
	v_mov_b32_dpp v52, v50 row_half_mirror row_mask:0xf bank_mask:0xf
	v_mov_b32_dpp v53, v51 row_half_mirror row_mask:0xf bank_mask:0xf
	s_waitcnt lgkmcnt(0)
	v_add_f64 v[50:51], v[50:51], v[52:53]
	s_nop 1
	v_mov_b32_dpp v52, v50 row_mirror row_mask:0xf bank_mask:0xf
	v_mov_b32_dpp v53, v51 row_mirror row_mask:0xf bank_mask:0xf
	s_and_saveexec_b64 s[0:1], vcc
	s_cbranch_execz .LBB2_168
	v_lshrrev_b32_e32 v0, 8, v105
	v_lshl_add_u32 v0, v0, 3, 0
	v_lshl_add_u32 v54, v104, 3, 0
	v_add_u32_e32 v0, 0x13450, v0
	v_add_u32_e32 v56, 0x12ed0, v54
	ds_read_b64 v[54:55], v0
	ds_read_b64 v[56:57], v56
	s_waitcnt lgkmcnt(2)
	v_add_f64 v[50:51], v[50:51], v[52:53]
	s_waitcnt lgkmcnt(1)
	v_mul_f64 v[50:51], v[50:51], v[54:55]
	s_waitcnt lgkmcnt(0)
	v_mul_f64 v[50:51], v[50:51], v[56:57]
	ds_write_b64 v101, v[50:51]
	s_branch .LBB2_168
